# speedup vs baseline: 1.0038x; 1.0038x over previous
.Lp2_polled:
	s_barrier
	v_mul_u32_u24_e32 v13, 0x880, v0
	global_load_dword v2, v13, s[24:25] sc1
	v_add_u32_e32 v14, 0x44000, v13
	global_load_dword v3, v14, s[24:25] sc1
	v_add_u32_e32 v14, 0x88000, v13
	global_load_dword v4, v14, s[24:25] sc1
	v_add_u32_e32 v14, 0xcc000, v13
	global_load_dword v5, v14, s[24:25] sc1
	v_add_u32_e32 v14, 0x110000, v13
	v_mov_b32_e32 v6, 0
	v_cmp_gt_u32_e32 vcc, 9, v0
	s_and_saveexec_b64 s[22:23], vcc
	global_load_dword v6, v14, s[24:25] sc1
	s_mov_b64 exec, s[22:23]
	v_mul_u32_u24_e32 v13, 0x1800, v0
	s_waitcnt vmcnt(0)
	v_lshrrev_b32_e32 v7, 16, v2
	v_and_b32_e32 v2, 0xffff, v2
	v_lshl_add_u32 v2, v2, 2, v13
	v_lshrrev_b32_e32 v8, 16, v3
	v_and_b32_e32 v3, 0xffff, v3
	v_add_u32_e32 v14, 0xc0000, v13
	v_lshl_add_u32 v3, v3, 2, v14
	v_lshrrev_b32_e32 v9, 16, v4
	v_and_b32_e32 v4, 0xffff, v4
	v_add_u32_e32 v14, 0x180000, v13
	v_lshl_add_u32 v4, v4, 2, v14
	v_lshrrev_b32_e32 v10, 16, v5
	v_and_b32_e32 v5, 0xffff, v5
	v_add_u32_e32 v14, 0x240000, v13
	v_lshl_add_u32 v5, v5, 2, v14
	v_lshrrev_b32_e32 v11, 16, v6
	v_and_b32_e32 v6, 0xffff, v6
	v_add_u32_e32 v14, 0x300000, v13
	v_lshl_add_u32 v6, v6, 2, v14
	v_cmp_lt_u32_e32 vcc, 0, v7
	s_and_saveexec_b64 s[22:23], vcc
	global_load_dwordx4 v[20:23], v2, s[26:27] sc1
	v_cmp_lt_u32_e32 vcc, 4, v7
	s_and_b64 exec, exec, vcc
	global_load_dwordx4 v[24:27], v2, s[26:27] offset:16 sc1
	s_mov_b64 exec, s[22:23]
	v_cmp_lt_u32_e32 vcc, 0, v8
	s_and_saveexec_b64 s[22:23], vcc
	global_load_dwordx4 v[28:31], v3, s[26:27] sc1
	v_cmp_lt_u32_e32 vcc, 4, v8
	s_and_b64 exec, exec, vcc
	global_load_dwordx4 v[32:35], v3, s[26:27] offset:16 sc1
	s_mov_b64 exec, s[22:23]
	v_cmp_lt_u32_e32 vcc, 0, v9
	s_and_saveexec_b64 s[22:23], vcc
	global_load_dwordx4 v[36:39], v4, s[26:27] sc1
	v_cmp_lt_u32_e32 vcc, 4, v9
	s_and_b64 exec, exec, vcc
	global_load_dwordx4 v[40:43], v4, s[26:27] offset:16 sc1
	s_mov_b64 exec, s[22:23]
	v_cmp_lt_u32_e32 vcc, 0, v10
	s_and_saveexec_b64 s[22:23], vcc
	global_load_dwordx4 v[44:47], v5, s[26:27] sc1
	v_cmp_lt_u32_e32 vcc, 4, v10
	s_and_b64 exec, exec, vcc
	global_load_dwordx4 v[48:51], v5, s[26:27] offset:16 sc1
	s_mov_b64 exec, s[22:23]
	v_cmp_lt_u32_e32 vcc, 0, v11
	s_and_saveexec_b64 s[22:23], vcc
	global_load_dwordx4 v[52:55], v6, s[26:27] sc1
	v_cmp_lt_u32_e32 vcc, 4, v11
	s_and_b64 exec, exec, vcc
	global_load_dwordx4 v[56:59], v6, s[26:27] offset:16 sc1
	s_mov_b64 exec, s[22:23]
	s_waitcnt vmcnt(0)
	v_cmp_lt_u32_e32 vcc, 0, v7
	s_and_saveexec_b64 s[22:23], vcc
	v_bfe_u32 v13, v20, 16, 7
	v_lshlrev_b32_e32 v13, 2, v13
	ds_add_rtn_u32 v60, v13, v12
	s_mov_b64 exec, s[22:23]
	v_cmp_lt_u32_e32 vcc, 1, v7
	s_and_saveexec_b64 s[22:23], vcc
	v_bfe_u32 v13, v21, 16, 7
	v_lshlrev_b32_e32 v13, 2, v13
	ds_add_rtn_u32 v61, v13, v12
	s_mov_b64 exec, s[22:23]
	v_cmp_lt_u32_e32 vcc, 2, v7
	s_and_saveexec_b64 s[22:23], vcc
	v_bfe_u32 v13, v22, 16, 7
	v_lshlrev_b32_e32 v13, 2, v13
	ds_add_rtn_u32 v62, v13, v12
	s_mov_b64 exec, s[22:23]
	v_cmp_lt_u32_e32 vcc, 3, v7
	s_and_saveexec_b64 s[22:23], vcc
	v_bfe_u32 v13, v23, 16, 7
	v_lshlrev_b32_e32 v13, 2, v13
	ds_add_rtn_u32 v63, v13, v12
	s_mov_b64 exec, s[22:23]
	v_cmp_lt_u32_e32 vcc, 4, v7
	s_cbranch_vccz .Lp2_c0_p1done
	s_and_saveexec_b64 s[22:23], vcc
	v_bfe_u32 v13, v24, 16, 7
	v_lshlrev_b32_e32 v13, 2, v13
	ds_add_rtn_u32 v64, v13, v12
	s_mov_b64 exec, s[22:23]
	v_cmp_lt_u32_e32 vcc, 5, v7
	s_cbranch_vccz .Lp2_c0_p1done
	s_and_saveexec_b64 s[22:23], vcc
	v_bfe_u32 v13, v25, 16, 7
	v_lshlrev_b32_e32 v13, 2, v13
	ds_add_rtn_u32 v65, v13, v12
	s_mov_b64 exec, s[22:23]
	v_cmp_lt_u32_e32 vcc, 6, v7
	s_cbranch_vccz .Lp2_c0_p1done
	s_and_saveexec_b64 s[22:23], vcc
	v_bfe_u32 v13, v26, 16, 7
	v_lshlrev_b32_e32 v13, 2, v13
	ds_add_rtn_u32 v66, v13, v12
	s_mov_b64 exec, s[22:23]
	v_cmp_lt_u32_e32 vcc, 7, v7
	s_cbranch_vccz .Lp2_c0_p1done
	s_and_saveexec_b64 s[22:23], vcc
	v_bfe_u32 v13, v27, 16, 7
	v_lshlrev_b32_e32 v13, 2, v13
	ds_add_rtn_u32 v67, v13, v12
	s_mov_b64 exec, s[22:23]
.Lp2_c0_p1done:
	s_waitcnt lgkmcnt(7)
	v_cmp_lt_u32_e32 vcc, 0, v8
	s_and_saveexec_b64 s[22:23], vcc
	v_bfe_u32 v13, v28, 16, 7
	v_lshlrev_b32_e32 v13, 2, v13
	ds_add_rtn_u32 v68, v13, v12
	s_mov_b64 exec, s[22:23]
	v_cmp_lt_u32_e32 vcc, 1, v8
	s_and_saveexec_b64 s[22:23], vcc
	v_bfe_u32 v13, v29, 16, 7
	v_lshlrev_b32_e32 v13, 2, v13
	ds_add_rtn_u32 v69, v13, v12
	s_mov_b64 exec, s[22:23]
	v_cmp_lt_u32_e32 vcc, 2, v8
	s_and_saveexec_b64 s[22:23], vcc
	v_bfe_u32 v13, v30, 16, 7
	v_lshlrev_b32_e32 v13, 2, v13
	ds_add_rtn_u32 v70, v13, v12
	s_mov_b64 exec, s[22:23]
	v_cmp_lt_u32_e32 vcc, 3, v8
	s_and_saveexec_b64 s[22:23], vcc
	v_bfe_u32 v13, v31, 16, 7
	v_lshlrev_b32_e32 v13, 2, v13
	ds_add_rtn_u32 v71, v13, v12
	s_mov_b64 exec, s[22:23]
	v_cmp_lt_u32_e32 vcc, 4, v8
	s_cbranch_vccz .Lp2_c1_p1done
	s_and_saveexec_b64 s[22:23], vcc
	v_bfe_u32 v13, v32, 16, 7
	v_lshlrev_b32_e32 v13, 2, v13
	ds_add_rtn_u32 v72, v13, v12
	s_mov_b64 exec, s[22:23]
	v_cmp_lt_u32_e32 vcc, 5, v8
	s_cbranch_vccz .Lp2_c1_p1done
	s_and_saveexec_b64 s[22:23], vcc
	v_bfe_u32 v13, v33, 16, 7
	v_lshlrev_b32_e32 v13, 2, v13
	ds_add_rtn_u32 v73, v13, v12
	s_mov_b64 exec, s[22:23]
	v_cmp_lt_u32_e32 vcc, 6, v8
	s_cbranch_vccz .Lp2_c1_p1done
	s_and_saveexec_b64 s[22:23], vcc
	v_bfe_u32 v13, v34, 16, 7
	v_lshlrev_b32_e32 v13, 2, v13
	ds_add_rtn_u32 v74, v13, v12
	s_mov_b64 exec, s[22:23]
	v_cmp_lt_u32_e32 vcc, 7, v8
	s_cbranch_vccz .Lp2_c1_p1done
	s_and_saveexec_b64 s[22:23], vcc
	v_bfe_u32 v13, v35, 16, 7
	v_lshlrev_b32_e32 v13, 2, v13
	ds_add_rtn_u32 v75, v13, v12
	s_mov_b64 exec, s[22:23]
.Lp2_c1_p1done:
	s_waitcnt lgkmcnt(7)
	v_cmp_lt_u32_e32 vcc, 0, v9
	s_and_saveexec_b64 s[22:23], vcc
	v_bfe_u32 v13, v36, 16, 7
	v_lshlrev_b32_e32 v13, 2, v13
	ds_add_rtn_u32 v76, v13, v12
	s_mov_b64 exec, s[22:23]
	v_cmp_lt_u32_e32 vcc, 1, v9
	s_and_saveexec_b64 s[22:23], vcc
	v_bfe_u32 v13, v37, 16, 7
	v_lshlrev_b32_e32 v13, 2, v13
	ds_add_rtn_u32 v77, v13, v12
	s_mov_b64 exec, s[22:23]
	v_cmp_lt_u32_e32 vcc, 2, v9
	s_and_saveexec_b64 s[22:23], vcc
	v_bfe_u32 v13, v38, 16, 7
	v_lshlrev_b32_e32 v13, 2, v13
	ds_add_rtn_u32 v78, v13, v12
	s_mov_b64 exec, s[22:23]
	v_cmp_lt_u32_e32 vcc, 3, v9
	s_and_saveexec_b64 s[22:23], vcc
	v_bfe_u32 v13, v39, 16, 7
	v_lshlrev_b32_e32 v13, 2, v13
	ds_add_rtn_u32 v79, v13, v12
	s_mov_b64 exec, s[22:23]
	v_cmp_lt_u32_e32 vcc, 4, v9
	s_cbranch_vccz .Lp2_c2_p1done
	s_and_saveexec_b64 s[22:23], vcc
	v_bfe_u32 v13, v40, 16, 7
	v_lshlrev_b32_e32 v13, 2, v13
	ds_add_rtn_u32 v80, v13, v12
	s_mov_b64 exec, s[22:23]
	v_cmp_lt_u32_e32 vcc, 5, v9
	s_cbranch_vccz .Lp2_c2_p1done
	s_and_saveexec_b64 s[22:23], vcc
	v_bfe_u32 v13, v41, 16, 7
	v_lshlrev_b32_e32 v13, 2, v13
	ds_add_rtn_u32 v81, v13, v12
	s_mov_b64 exec, s[22:23]
	v_cmp_lt_u32_e32 vcc, 6, v9
	s_cbranch_vccz .Lp2_c2_p1done
	s_and_saveexec_b64 s[22:23], vcc
	v_bfe_u32 v13, v42, 16, 7
	v_lshlrev_b32_e32 v13, 2, v13
	ds_add_rtn_u32 v82, v13, v12
	s_mov_b64 exec, s[22:23]
	v_cmp_lt_u32_e32 vcc, 7, v9
	s_cbranch_vccz .Lp2_c2_p1done
	s_and_saveexec_b64 s[22:23], vcc
	v_bfe_u32 v13, v43, 16, 7
	v_lshlrev_b32_e32 v13, 2, v13
	ds_add_rtn_u32 v83, v13, v12
	s_mov_b64 exec, s[22:23]
.Lp2_c2_p1done:
	s_waitcnt lgkmcnt(7)
	v_cmp_lt_u32_e32 vcc, 0, v10
	s_and_saveexec_b64 s[22:23], vcc
	v_bfe_u32 v13, v44, 16, 7
	v_lshlrev_b32_e32 v13, 2, v13
	ds_add_rtn_u32 v84, v13, v12
	s_mov_b64 exec, s[22:23]
	v_cmp_lt_u32_e32 vcc, 1, v10
	s_and_saveexec_b64 s[22:23], vcc
	v_bfe_u32 v13, v45, 16, 7
	v_lshlrev_b32_e32 v13, 2, v13
	ds_add_rtn_u32 v85, v13, v12
	s_mov_b64 exec, s[22:23]
	v_cmp_lt_u32_e32 vcc, 2, v10
	s_and_saveexec_b64 s[22:23], vcc
	v_bfe_u32 v13, v46, 16, 7
	v_lshlrev_b32_e32 v13, 2, v13
	ds_add_rtn_u32 v86, v13, v12
	s_mov_b64 exec, s[22:23]
	v_cmp_lt_u32_e32 vcc, 3, v10
	s_and_saveexec_b64 s[22:23], vcc
	v_bfe_u32 v13, v47, 16, 7
	v_lshlrev_b32_e32 v13, 2, v13
	ds_add_rtn_u32 v87, v13, v12
	s_mov_b64 exec, s[22:23]
	v_cmp_lt_u32_e32 vcc, 4, v10
	s_cbranch_vccz .Lp2_c3_p1done
	s_and_saveexec_b64 s[22:23], vcc
	v_bfe_u32 v13, v48, 16, 7
	v_lshlrev_b32_e32 v13, 2, v13
	ds_add_rtn_u32 v88, v13, v12
	s_mov_b64 exec, s[22:23]
	v_cmp_lt_u32_e32 vcc, 5, v10
	s_cbranch_vccz .Lp2_c3_p1done
	s_and_saveexec_b64 s[22:23], vcc
	v_bfe_u32 v13, v49, 16, 7
	v_lshlrev_b32_e32 v13, 2, v13
	ds_add_rtn_u32 v89, v13, v12
	s_mov_b64 exec, s[22:23]
	v_cmp_lt_u32_e32 vcc, 6, v10
	s_cbranch_vccz .Lp2_c3_p1done
	s_and_saveexec_b64 s[22:23], vcc
	v_bfe_u32 v13, v50, 16, 7
	v_lshlrev_b32_e32 v13, 2, v13
	ds_add_rtn_u32 v90, v13, v12
	s_mov_b64 exec, s[22:23]
	v_cmp_lt_u32_e32 vcc, 7, v10
	s_cbranch_vccz .Lp2_c3_p1done
	s_and_saveexec_b64 s[22:23], vcc
	v_bfe_u32 v13, v51, 16, 7
	v_lshlrev_b32_e32 v13, 2, v13
	ds_add_rtn_u32 v91, v13, v12
	s_mov_b64 exec, s[22:23]
.Lp2_c3_p1done:
	s_waitcnt lgkmcnt(0)
	v_cmp_lt_u32_e32 vcc, 0, v7
	s_and_saveexec_b64 s[22:23], vcc
	v_cmp_gt_u32_e32 vcc, 32, v60
	s_andn2_b64 s[36:37], exec, vcc
	s_or_b64 s[38:39], s[38:39], s[36:37]
	s_and_b64 exec, exec, vcc
	v_lshrrev_b32_e32 v13, 16, v20
	v_lshl_add_u32 v13, v13, 5, v60
	v_lshlrev_b32_e32 v13, 2, v13
	v_and_b32_e32 v14, 0xffff, v20
	global_store_dword v13, v14, s[6:7] sc1
	s_mov_b64 exec, s[22:23]
	v_cmp_lt_u32_e32 vcc, 1, v7
	s_and_saveexec_b64 s[22:23], vcc
	v_cmp_gt_u32_e32 vcc, 32, v61
	s_andn2_b64 s[36:37], exec, vcc
	s_or_b64 s[38:39], s[38:39], s[36:37]
	s_and_b64 exec, exec, vcc
	v_lshrrev_b32_e32 v13, 16, v21
	v_lshl_add_u32 v13, v13, 5, v61
	v_lshlrev_b32_e32 v13, 2, v13
	v_and_b32_e32 v14, 0xffff, v21
	global_store_dword v13, v14, s[6:7] sc1
	s_mov_b64 exec, s[22:23]
	v_cmp_lt_u32_e32 vcc, 2, v7
	s_and_saveexec_b64 s[22:23], vcc
	v_cmp_gt_u32_e32 vcc, 32, v62
	s_andn2_b64 s[36:37], exec, vcc
	s_or_b64 s[38:39], s[38:39], s[36:37]
	s_and_b64 exec, exec, vcc
	v_lshrrev_b32_e32 v13, 16, v22
	v_lshl_add_u32 v13, v13, 5, v62
	v_lshlrev_b32_e32 v13, 2, v13
	v_and_b32_e32 v14, 0xffff, v22
	global_store_dword v13, v14, s[6:7] sc1
	s_mov_b64 exec, s[22:23]
	v_cmp_lt_u32_e32 vcc, 3, v7
	s_and_saveexec_b64 s[22:23], vcc
	v_cmp_gt_u32_e32 vcc, 32, v63
	s_andn2_b64 s[36:37], exec, vcc
	s_or_b64 s[38:39], s[38:39], s[36:37]
	s_and_b64 exec, exec, vcc
	v_lshrrev_b32_e32 v13, 16, v23
	v_lshl_add_u32 v13, v13, 5, v63
	v_lshlrev_b32_e32 v13, 2, v13
	v_and_b32_e32 v14, 0xffff, v23
	global_store_dword v13, v14, s[6:7] sc1
	s_mov_b64 exec, s[22:23]
	v_cmp_lt_u32_e32 vcc, 4, v7
	s_cbranch_vccz .Lp2_c0_p2done
	s_and_saveexec_b64 s[22:23], vcc
	v_cmp_gt_u32_e32 vcc, 32, v64
	s_andn2_b64 s[36:37], exec, vcc
	s_or_b64 s[38:39], s[38:39], s[36:37]
	s_and_b64 exec, exec, vcc
	v_lshrrev_b32_e32 v13, 16, v24
	v_lshl_add_u32 v13, v13, 5, v64
	v_lshlrev_b32_e32 v13, 2, v13
	v_and_b32_e32 v14, 0xffff, v24
	global_store_dword v13, v14, s[6:7] sc1
	s_mov_b64 exec, s[22:23]
	v_cmp_lt_u32_e32 vcc, 5, v7
	s_cbranch_vccz .Lp2_c0_p2done
	s_and_saveexec_b64 s[22:23], vcc
	v_cmp_gt_u32_e32 vcc, 32, v65
	s_andn2_b64 s[36:37], exec, vcc
	s_or_b64 s[38:39], s[38:39], s[36:37]
	s_and_b64 exec, exec, vcc
	v_lshrrev_b32_e32 v13, 16, v25
	v_lshl_add_u32 v13, v13, 5, v65
	v_lshlrev_b32_e32 v13, 2, v13
	v_and_b32_e32 v14, 0xffff, v25
	global_store_dword v13, v14, s[6:7] sc1
	s_mov_b64 exec, s[22:23]
	v_cmp_lt_u32_e32 vcc, 6, v7
	s_cbranch_vccz .Lp2_c0_p2done
	s_and_saveexec_b64 s[22:23], vcc
	v_cmp_gt_u32_e32 vcc, 32, v66
	s_andn2_b64 s[36:37], exec, vcc
	s_or_b64 s[38:39], s[38:39], s[36:37]
	s_and_b64 exec, exec, vcc
	v_lshrrev_b32_e32 v13, 16, v26
	v_lshl_add_u32 v13, v13, 5, v66
	v_lshlrev_b32_e32 v13, 2, v13
	v_and_b32_e32 v14, 0xffff, v26
	global_store_dword v13, v14, s[6:7] sc1
	s_mov_b64 exec, s[22:23]
	v_cmp_lt_u32_e32 vcc, 7, v7
	s_cbranch_vccz .Lp2_c0_p2done
	s_and_saveexec_b64 s[22:23], vcc
	v_cmp_gt_u32_e32 vcc, 32, v67
	s_andn2_b64 s[36:37], exec, vcc
	s_or_b64 s[38:39], s[38:39], s[36:37]
	s_and_b64 exec, exec, vcc
	v_lshrrev_b32_e32 v13, 16, v27
	v_lshl_add_u32 v13, v13, 5, v67
	v_lshlrev_b32_e32 v13, 2, v13
	v_and_b32_e32 v14, 0xffff, v27
	global_store_dword v13, v14, s[6:7] sc1
	s_mov_b64 exec, s[22:23]
.Lp2_c0_p2done:
	v_cmp_lt_u32_e32 vcc, 0, v8
	s_and_saveexec_b64 s[22:23], vcc
	v_cmp_gt_u32_e32 vcc, 32, v68
	s_andn2_b64 s[36:37], exec, vcc
	s_or_b64 s[38:39], s[38:39], s[36:37]
	s_and_b64 exec, exec, vcc
	v_lshrrev_b32_e32 v13, 16, v28
	v_lshl_add_u32 v13, v13, 5, v68
	v_lshlrev_b32_e32 v13, 2, v13
	v_and_b32_e32 v14, 0xffff, v28
	global_store_dword v13, v14, s[6:7] sc1
	s_mov_b64 exec, s[22:23]
	v_cmp_lt_u32_e32 vcc, 1, v8
	s_and_saveexec_b64 s[22:23], vcc
	v_cmp_gt_u32_e32 vcc, 32, v69
	s_andn2_b64 s[36:37], exec, vcc
	s_or_b64 s[38:39], s[38:39], s[36:37]
	s_and_b64 exec, exec, vcc
	v_lshrrev_b32_e32 v13, 16, v29
	v_lshl_add_u32 v13, v13, 5, v69
	v_lshlrev_b32_e32 v13, 2, v13
	v_and_b32_e32 v14, 0xffff, v29
	global_store_dword v13, v14, s[6:7] sc1
	s_mov_b64 exec, s[22:23]
	v_cmp_lt_u32_e32 vcc, 2, v8
	s_and_saveexec_b64 s[22:23], vcc
	v_cmp_gt_u32_e32 vcc, 32, v70
	s_andn2_b64 s[36:37], exec, vcc
	s_or_b64 s[38:39], s[38:39], s[36:37]
	s_and_b64 exec, exec, vcc
	v_lshrrev_b32_e32 v13, 16, v30
	v_lshl_add_u32 v13, v13, 5, v70
	v_lshlrev_b32_e32 v13, 2, v13
	v_and_b32_e32 v14, 0xffff, v30
	global_store_dword v13, v14, s[6:7] sc1
	s_mov_b64 exec, s[22:23]
	v_cmp_lt_u32_e32 vcc, 3, v8
	s_and_saveexec_b64 s[22:23], vcc
	v_cmp_gt_u32_e32 vcc, 32, v71
	s_andn2_b64 s[36:37], exec, vcc
	s_or_b64 s[38:39], s[38:39], s[36:37]
	s_and_b64 exec, exec, vcc
	v_lshrrev_b32_e32 v13, 16, v31
	v_lshl_add_u32 v13, v13, 5, v71
	v_lshlrev_b32_e32 v13, 2, v13
	v_and_b32_e32 v14, 0xffff, v31
	global_store_dword v13, v14, s[6:7] sc1
	s_mov_b64 exec, s[22:23]
	v_cmp_lt_u32_e32 vcc, 4, v8
	s_cbranch_vccz .Lp2_c1_p2done
	s_and_saveexec_b64 s[22:23], vcc
	v_cmp_gt_u32_e32 vcc, 32, v72
	s_andn2_b64 s[36:37], exec, vcc
	s_or_b64 s[38:39], s[38:39], s[36:37]
	s_and_b64 exec, exec, vcc
	v_lshrrev_b32_e32 v13, 16, v32
	v_lshl_add_u32 v13, v13, 5, v72
	v_lshlrev_b32_e32 v13, 2, v13
	v_and_b32_e32 v14, 0xffff, v32
	global_store_dword v13, v14, s[6:7] sc1
	s_mov_b64 exec, s[22:23]
	v_cmp_lt_u32_e32 vcc, 5, v8
	s_cbranch_vccz .Lp2_c1_p2done
	s_and_saveexec_b64 s[22:23], vcc
	v_cmp_gt_u32_e32 vcc, 32, v73
	s_andn2_b64 s[36:37], exec, vcc
	s_or_b64 s[38:39], s[38:39], s[36:37]
	s_and_b64 exec, exec, vcc
	v_lshrrev_b32_e32 v13, 16, v33
	v_lshl_add_u32 v13, v13, 5, v73
	v_lshlrev_b32_e32 v13, 2, v13
	v_and_b32_e32 v14, 0xffff, v33
	global_store_dword v13, v14, s[6:7] sc1
	s_mov_b64 exec, s[22:23]
	v_cmp_lt_u32_e32 vcc, 6, v8
	s_cbranch_vccz .Lp2_c1_p2done
	s_and_saveexec_b64 s[22:23], vcc
	v_cmp_gt_u32_e32 vcc, 32, v74
	s_andn2_b64 s[36:37], exec, vcc
	s_or_b64 s[38:39], s[38:39], s[36:37]
	s_and_b64 exec, exec, vcc
	v_lshrrev_b32_e32 v13, 16, v34
	v_lshl_add_u32 v13, v13, 5, v74
	v_lshlrev_b32_e32 v13, 2, v13
	v_and_b32_e32 v14, 0xffff, v34
	global_store_dword v13, v14, s[6:7] sc1
	s_mov_b64 exec, s[22:23]
	v_cmp_lt_u32_e32 vcc, 7, v8
	s_cbranch_vccz .Lp2_c1_p2done
	s_and_saveexec_b64 s[22:23], vcc
	v_cmp_gt_u32_e32 vcc, 32, v75
	s_andn2_b64 s[36:37], exec, vcc
	s_or_b64 s[38:39], s[38:39], s[36:37]
	s_and_b64 exec, exec, vcc
	v_lshrrev_b32_e32 v13, 16, v35
	v_lshl_add_u32 v13, v13, 5, v75
	v_lshlrev_b32_e32 v13, 2, v13
	v_and_b32_e32 v14, 0xffff, v35
	global_store_dword v13, v14, s[6:7] sc1
	s_mov_b64 exec, s[22:23]
.Lp2_c1_p2done:
	v_cmp_lt_u32_e32 vcc, 0, v9
	s_and_saveexec_b64 s[22:23], vcc
	v_cmp_gt_u32_e32 vcc, 32, v76
	s_andn2_b64 s[36:37], exec, vcc
	s_or_b64 s[38:39], s[38:39], s[36:37]
	s_and_b64 exec, exec, vcc
	v_lshrrev_b32_e32 v13, 16, v36
	v_lshl_add_u32 v13, v13, 5, v76
	v_lshlrev_b32_e32 v13, 2, v13
	v_and_b32_e32 v14, 0xffff, v36
	global_store_dword v13, v14, s[6:7] sc1
	s_mov_b64 exec, s[22:23]
	v_cmp_lt_u32_e32 vcc, 1, v9
	s_and_saveexec_b64 s[22:23], vcc
	v_cmp_gt_u32_e32 vcc, 32, v77
	s_andn2_b64 s[36:37], exec, vcc
	s_or_b64 s[38:39], s[38:39], s[36:37]
	s_and_b64 exec, exec, vcc
	v_lshrrev_b32_e32 v13, 16, v37
	v_lshl_add_u32 v13, v13, 5, v77
	v_lshlrev_b32_e32 v13, 2, v13
	v_and_b32_e32 v14, 0xffff, v37
	global_store_dword v13, v14, s[6:7] sc1
	s_mov_b64 exec, s[22:23]
	v_cmp_lt_u32_e32 vcc, 2, v9
	s_and_saveexec_b64 s[22:23], vcc
	v_cmp_gt_u32_e32 vcc, 32, v78
	s_andn2_b64 s[36:37], exec, vcc
	s_or_b64 s[38:39], s[38:39], s[36:37]
	s_and_b64 exec, exec, vcc
	v_lshrrev_b32_e32 v13, 16, v38
	v_lshl_add_u32 v13, v13, 5, v78
	v_lshlrev_b32_e32 v13, 2, v13
	v_and_b32_e32 v14, 0xffff, v38
	global_store_dword v13, v14, s[6:7] sc1
	s_mov_b64 exec, s[22:23]
	v_cmp_lt_u32_e32 vcc, 3, v9
	s_and_saveexec_b64 s[22:23], vcc
	v_cmp_gt_u32_e32 vcc, 32, v79
	s_andn2_b64 s[36:37], exec, vcc
	s_or_b64 s[38:39], s[38:39], s[36:37]
	s_and_b64 exec, exec, vcc
	v_lshrrev_b32_e32 v13, 16, v39
	v_lshl_add_u32 v13, v13, 5, v79
	v_lshlrev_b32_e32 v13, 2, v13
	v_and_b32_e32 v14, 0xffff, v39
	global_store_dword v13, v14, s[6:7] sc1
	s_mov_b64 exec, s[22:23]
	v_cmp_lt_u32_e32 vcc, 4, v9
	s_cbranch_vccz .Lp2_c2_p2done
	s_and_saveexec_b64 s[22:23], vcc
	v_cmp_gt_u32_e32 vcc, 32, v80
	s_andn2_b64 s[36:37], exec, vcc
	s_or_b64 s[38:39], s[38:39], s[36:37]
	s_and_b64 exec, exec, vcc
	v_lshrrev_b32_e32 v13, 16, v40
	v_lshl_add_u32 v13, v13, 5, v80
	v_lshlrev_b32_e32 v13, 2, v13
	v_and_b32_e32 v14, 0xffff, v40
	global_store_dword v13, v14, s[6:7] sc1
	s_mov_b64 exec, s[22:23]
	v_cmp_lt_u32_e32 vcc, 5, v9
	s_cbranch_vccz .Lp2_c2_p2done
	s_and_saveexec_b64 s[22:23], vcc
	v_cmp_gt_u32_e32 vcc, 32, v81
	s_andn2_b64 s[36:37], exec, vcc
	s_or_b64 s[38:39], s[38:39], s[36:37]
	s_and_b64 exec, exec, vcc
	v_lshrrev_b32_e32 v13, 16, v41
	v_lshl_add_u32 v13, v13, 5, v81
	v_lshlrev_b32_e32 v13, 2, v13
	v_and_b32_e32 v14, 0xffff, v41
	global_store_dword v13, v14, s[6:7] sc1
	s_mov_b64 exec, s[22:23]
	v_cmp_lt_u32_e32 vcc, 6, v9
	s_cbranch_vccz .Lp2_c2_p2done
	s_and_saveexec_b64 s[22:23], vcc
	v_cmp_gt_u32_e32 vcc, 32, v82
	s_andn2_b64 s[36:37], exec, vcc
	s_or_b64 s[38:39], s[38:39], s[36:37]
	s_and_b64 exec, exec, vcc
	v_lshrrev_b32_e32 v13, 16, v42
	v_lshl_add_u32 v13, v13, 5, v82
	v_lshlrev_b32_e32 v13, 2, v13
	v_and_b32_e32 v14, 0xffff, v42
	global_store_dword v13, v14, s[6:7] sc1
	s_mov_b64 exec, s[22:23]
	v_cmp_lt_u32_e32 vcc, 7, v9
	s_cbranch_vccz .Lp2_c2_p2done
	s_and_saveexec_b64 s[22:23], vcc
	v_cmp_gt_u32_e32 vcc, 32, v83
	s_andn2_b64 s[36:37], exec, vcc
	s_or_b64 s[38:39], s[38:39], s[36:37]
	s_and_b64 exec, exec, vcc
	v_lshrrev_b32_e32 v13, 16, v43
	v_lshl_add_u32 v13, v13, 5, v83
	v_lshlrev_b32_e32 v13, 2, v13
	v_and_b32_e32 v14, 0xffff, v43
	global_store_dword v13, v14, s[6:7] sc1
	s_mov_b64 exec, s[22:23]
.Lp2_c2_p2done:
	v_cmp_lt_u32_e32 vcc, 0, v10
	s_and_saveexec_b64 s[22:23], vcc
	v_cmp_gt_u32_e32 vcc, 32, v84
	s_andn2_b64 s[36:37], exec, vcc
	s_or_b64 s[38:39], s[38:39], s[36:37]
	s_and_b64 exec, exec, vcc
	v_lshrrev_b32_e32 v13, 16, v44
	v_lshl_add_u32 v13, v13, 5, v84
	v_lshlrev_b32_e32 v13, 2, v13
	v_and_b32_e32 v14, 0xffff, v44
	global_store_dword v13, v14, s[6:7] sc1
	s_mov_b64 exec, s[22:23]
	v_cmp_lt_u32_e32 vcc, 1, v10
	s_and_saveexec_b64 s[22:23], vcc
	v_cmp_gt_u32_e32 vcc, 32, v85
	s_andn2_b64 s[36:37], exec, vcc
	s_or_b64 s[38:39], s[38:39], s[36:37]
	s_and_b64 exec, exec, vcc
	v_lshrrev_b32_e32 v13, 16, v45
	v_lshl_add_u32 v13, v13, 5, v85
	v_lshlrev_b32_e32 v13, 2, v13
	v_and_b32_e32 v14, 0xffff, v45
	global_store_dword v13, v14, s[6:7] sc1
	s_mov_b64 exec, s[22:23]
	v_cmp_lt_u32_e32 vcc, 2, v10
	s_and_saveexec_b64 s[22:23], vcc
	v_cmp_gt_u32_e32 vcc, 32, v86
	s_andn2_b64 s[36:37], exec, vcc
	s_or_b64 s[38:39], s[38:39], s[36:37]
	s_and_b64 exec, exec, vcc
	v_lshrrev_b32_e32 v13, 16, v46
	v_lshl_add_u32 v13, v13, 5, v86
	v_lshlrev_b32_e32 v13, 2, v13
	v_and_b32_e32 v14, 0xffff, v46
	global_store_dword v13, v14, s[6:7] sc1
	s_mov_b64 exec, s[22:23]
	v_cmp_lt_u32_e32 vcc, 3, v10
	s_and_saveexec_b64 s[22:23], vcc
	v_cmp_gt_u32_e32 vcc, 32, v87
	s_andn2_b64 s[36:37], exec, vcc
	s_or_b64 s[38:39], s[38:39], s[36:37]
	s_and_b64 exec, exec, vcc
	v_lshrrev_b32_e32 v13, 16, v47
	v_lshl_add_u32 v13, v13, 5, v87
	v_lshlrev_b32_e32 v13, 2, v13
	v_and_b32_e32 v14, 0xffff, v47
	global_store_dword v13, v14, s[6:7] sc1
	s_mov_b64 exec, s[22:23]
	v_cmp_lt_u32_e32 vcc, 4, v10
	s_cbranch_vccz .Lp2_c3_p2done
	s_and_saveexec_b64 s[22:23], vcc
	v_cmp_gt_u32_e32 vcc, 32, v88
	s_andn2_b64 s[36:37], exec, vcc
	s_or_b64 s[38:39], s[38:39], s[36:37]
	s_and_b64 exec, exec, vcc
	v_lshrrev_b32_e32 v13, 16, v48
	v_lshl_add_u32 v13, v13, 5, v88
	v_lshlrev_b32_e32 v13, 2, v13
	v_and_b32_e32 v14, 0xffff, v48
	global_store_dword v13, v14, s[6:7] sc1
	s_mov_b64 exec, s[22:23]
	v_cmp_lt_u32_e32 vcc, 5, v10
	s_cbranch_vccz .Lp2_c3_p2done
	s_and_saveexec_b64 s[22:23], vcc
	v_cmp_gt_u32_e32 vcc, 32, v89
	s_andn2_b64 s[36:37], exec, vcc
	s_or_b64 s[38:39], s[38:39], s[36:37]
	s_and_b64 exec, exec, vcc
	v_lshrrev_b32_e32 v13, 16, v49
	v_lshl_add_u32 v13, v13, 5, v89
	v_lshlrev_b32_e32 v13, 2, v13
	v_and_b32_e32 v14, 0xffff, v49
	global_store_dword v13, v14, s[6:7] sc1
	s_mov_b64 exec, s[22:23]
	v_cmp_lt_u32_e32 vcc, 6, v10
	s_cbranch_vccz .Lp2_c3_p2done
	s_and_saveexec_b64 s[22:23], vcc
	v_cmp_gt_u32_e32 vcc, 32, v90
	s_andn2_b64 s[36:37], exec, vcc
	s_or_b64 s[38:39], s[38:39], s[36:37]
	s_and_b64 exec, exec, vcc
	v_lshrrev_b32_e32 v13, 16, v50
	v_lshl_add_u32 v13, v13, 5, v90
	v_lshlrev_b32_e32 v13, 2, v13
	v_and_b32_e32 v14, 0xffff, v50
	global_store_dword v13, v14, s[6:7] sc1
	s_mov_b64 exec, s[22:23]
	v_cmp_lt_u32_e32 vcc, 7, v10
	s_cbranch_vccz .Lp2_c3_p2done
	s_and_saveexec_b64 s[22:23], vcc
	v_cmp_gt_u32_e32 vcc, 32, v91
	s_andn2_b64 s[36:37], exec, vcc
	s_or_b64 s[38:39], s[38:39], s[36:37]
	s_and_b64 exec, exec, vcc
	v_lshrrev_b32_e32 v13, 16, v51
	v_lshl_add_u32 v13, v13, 5, v91
	v_lshlrev_b32_e32 v13, 2, v13
	v_and_b32_e32 v14, 0xffff, v51
	global_store_dword v13, v14, s[6:7] sc1
	s_mov_b64 exec, s[22:23]
.Lp2_c3_p2done:
	v_cmp_lt_u32_e32 vcc, 0, v11
	s_and_saveexec_b64 s[22:23], vcc
	v_bfe_u32 v13, v52, 16, 7
	v_lshlrev_b32_e32 v13, 2, v13
	ds_add_rtn_u32 v60, v13, v12
	s_mov_b64 exec, s[22:23]
	v_cmp_lt_u32_e32 vcc, 1, v11
	s_and_saveexec_b64 s[22:23], vcc
	v_bfe_u32 v13, v53, 16, 7
	v_lshlrev_b32_e32 v13, 2, v13
	ds_add_rtn_u32 v61, v13, v12
	s_mov_b64 exec, s[22:23]
	v_cmp_lt_u32_e32 vcc, 2, v11
	s_and_saveexec_b64 s[22:23], vcc
	v_bfe_u32 v13, v54, 16, 7
	v_lshlrev_b32_e32 v13, 2, v13
	ds_add_rtn_u32 v62, v13, v12
	s_mov_b64 exec, s[22:23]
	v_cmp_lt_u32_e32 vcc, 3, v11
	s_and_saveexec_b64 s[22:23], vcc
	v_bfe_u32 v13, v55, 16, 7
	v_lshlrev_b32_e32 v13, 2, v13
	ds_add_rtn_u32 v63, v13, v12
	s_mov_b64 exec, s[22:23]
	v_cmp_lt_u32_e32 vcc, 4, v11
	s_cbranch_vccz .Lp2_c4_p1done
	s_and_saveexec_b64 s[22:23], vcc
	v_bfe_u32 v13, v56, 16, 7
	v_lshlrev_b32_e32 v13, 2, v13
	ds_add_rtn_u32 v64, v13, v12
	s_mov_b64 exec, s[22:23]
	v_cmp_lt_u32_e32 vcc, 5, v11
	s_cbranch_vccz .Lp2_c4_p1done
	s_and_saveexec_b64 s[22:23], vcc
	v_bfe_u32 v13, v57, 16, 7
	v_lshlrev_b32_e32 v13, 2, v13
	ds_add_rtn_u32 v65, v13, v12
	s_mov_b64 exec, s[22:23]
	v_cmp_lt_u32_e32 vcc, 6, v11
	s_cbranch_vccz .Lp2_c4_p1done
	s_and_saveexec_b64 s[22:23], vcc
	v_bfe_u32 v13, v58, 16, 7
	v_lshlrev_b32_e32 v13, 2, v13
	ds_add_rtn_u32 v66, v13, v12
	s_mov_b64 exec, s[22:23]
	v_cmp_lt_u32_e32 vcc, 7, v11
	s_cbranch_vccz .Lp2_c4_p1done
	s_and_saveexec_b64 s[22:23], vcc
	v_bfe_u32 v13, v59, 16, 7
	v_lshlrev_b32_e32 v13, 2, v13
	ds_add_rtn_u32 v67, v13, v12
	s_mov_b64 exec, s[22:23]
.Lp2_c4_p1done:
	s_waitcnt lgkmcnt(0)
	v_cmp_lt_u32_e32 vcc, 0, v11
	s_and_saveexec_b64 s[22:23], vcc
	v_cmp_gt_u32_e32 vcc, 32, v60
	s_andn2_b64 s[36:37], exec, vcc
	s_or_b64 s[38:39], s[38:39], s[36:37]
	s_and_b64 exec, exec, vcc
	v_lshrrev_b32_e32 v13, 16, v52
	v_lshl_add_u32 v13, v13, 5, v60
	v_lshlrev_b32_e32 v13, 2, v13
	v_and_b32_e32 v14, 0xffff, v52
	global_store_dword v13, v14, s[6:7] sc1
	s_mov_b64 exec, s[22:23]
	v_cmp_lt_u32_e32 vcc, 1, v11
	s_and_saveexec_b64 s[22:23], vcc
	v_cmp_gt_u32_e32 vcc, 32, v61
	s_andn2_b64 s[36:37], exec, vcc
	s_or_b64 s[38:39], s[38:39], s[36:37]
	s_and_b64 exec, exec, vcc
	v_lshrrev_b32_e32 v13, 16, v53
	v_lshl_add_u32 v13, v13, 5, v61
	v_lshlrev_b32_e32 v13, 2, v13
	v_and_b32_e32 v14, 0xffff, v53
	global_store_dword v13, v14, s[6:7] sc1
	s_mov_b64 exec, s[22:23]
	v_cmp_lt_u32_e32 vcc, 2, v11
	s_and_saveexec_b64 s[22:23], vcc
	v_cmp_gt_u32_e32 vcc, 32, v62
	s_andn2_b64 s[36:37], exec, vcc
	s_or_b64 s[38:39], s[38:39], s[36:37]
	s_and_b64 exec, exec, vcc
	v_lshrrev_b32_e32 v13, 16, v54
	v_lshl_add_u32 v13, v13, 5, v62
	v_lshlrev_b32_e32 v13, 2, v13
	v_and_b32_e32 v14, 0xffff, v54
	global_store_dword v13, v14, s[6:7] sc1
	s_mov_b64 exec, s[22:23]
	v_cmp_lt_u32_e32 vcc, 3, v11
	s_and_saveexec_b64 s[22:23], vcc
	v_cmp_gt_u32_e32 vcc, 32, v63
	s_andn2_b64 s[36:37], exec, vcc
	s_or_b64 s[38:39], s[38:39], s[36:37]
	s_and_b64 exec, exec, vcc
	v_lshrrev_b32_e32 v13, 16, v55
	v_lshl_add_u32 v13, v13, 5, v63
	v_lshlrev_b32_e32 v13, 2, v13
	v_and_b32_e32 v14, 0xffff, v55
	global_store_dword v13, v14, s[6:7] sc1
	s_mov_b64 exec, s[22:23]
	v_cmp_lt_u32_e32 vcc, 4, v11
	s_cbranch_vccz .Lp2_c4_p2done
	s_and_saveexec_b64 s[22:23], vcc
	v_cmp_gt_u32_e32 vcc, 32, v64
	s_andn2_b64 s[36:37], exec, vcc
	s_or_b64 s[38:39], s[38:39], s[36:37]
	s_and_b64 exec, exec, vcc
	v_lshrrev_b32_e32 v13, 16, v56
	v_lshl_add_u32 v13, v13, 5, v64
	v_lshlrev_b32_e32 v13, 2, v13
	v_and_b32_e32 v14, 0xffff, v56
	global_store_dword v13, v14, s[6:7] sc1
	s_mov_b64 exec, s[22:23]
	v_cmp_lt_u32_e32 vcc, 5, v11
	s_cbranch_vccz .Lp2_c4_p2done
	s_and_saveexec_b64 s[22:23], vcc
	v_cmp_gt_u32_e32 vcc, 32, v65
	s_andn2_b64 s[36:37], exec, vcc
	s_or_b64 s[38:39], s[38:39], s[36:37]
	s_and_b64 exec, exec, vcc
	v_lshrrev_b32_e32 v13, 16, v57
	v_lshl_add_u32 v13, v13, 5, v65
	v_lshlrev_b32_e32 v13, 2, v13
	v_and_b32_e32 v14, 0xffff, v57
	global_store_dword v13, v14, s[6:7] sc1
	s_mov_b64 exec, s[22:23]
	v_cmp_lt_u32_e32 vcc, 6, v11
	s_cbranch_vccz .Lp2_c4_p2done
	s_and_saveexec_b64 s[22:23], vcc
	v_cmp_gt_u32_e32 vcc, 32, v66
	s_andn2_b64 s[36:37], exec, vcc
	s_or_b64 s[38:39], s[38:39], s[36:37]
	s_and_b64 exec, exec, vcc
	v_lshrrev_b32_e32 v13, 16, v58
	v_lshl_add_u32 v13, v13, 5, v66
	v_lshlrev_b32_e32 v13, 2, v13
	v_and_b32_e32 v14, 0xffff, v58
	global_store_dword v13, v14, s[6:7] sc1
	s_mov_b64 exec, s[22:23]
	v_cmp_lt_u32_e32 vcc, 7, v11
	s_cbranch_vccz .Lp2_c4_p2done
	s_and_saveexec_b64 s[22:23], vcc
	v_cmp_gt_u32_e32 vcc, 32, v67
	s_andn2_b64 s[36:37], exec, vcc
	s_or_b64 s[38:39], s[38:39], s[36:37]
	s_and_b64 exec, exec, vcc
	v_lshrrev_b32_e32 v13, 16, v59
	v_lshl_add_u32 v13, v13, 5, v67
	v_lshlrev_b32_e32 v13, 2, v13
	v_and_b32_e32 v14, 0xffff, v59
	global_store_dword v13, v14, s[6:7] sc1
	s_mov_b64 exec, s[22:23]
